# speedup vs baseline: 1.0028x; 1.0028x over previous
.LBB1_5:
	s_waitcnt lgkmcnt(6)
	v_mfma_f32_32x32x64_f8f6f4 v[4:19], v[156:163], v[148:155], v[4:19]
	v_cmp_eq_u32_e32 vcc, 0, v1
	s_nop 1
	s_and_saveexec_b64 s[0:1], vcc
	s_lshl_b32 s12, s29, 2
	s_add_i32 s12, s12, 0x12000
	v_mov_b32_e32 v1, s12
	ds_write_b32 v1, v0
	s_or_b64 exec, exec, s[0:1]
	s_waitcnt vmcnt(0) lgkmcnt(0)
	s_barrier
	s_cmp_lt_u32 s29, 4
	s_cbranch_scc0 .Lprio_skip
	s_setprio 2
.Lprio_skip:
	v_mov_b32_e32 v104, 0
	v_mov_b32_e32 v206, 0x12000
	ds_read_b128 v[38:41], v206
	ds_read_b128 v[42:45], v206 offset:16
	s_mov_b32 s14, 0
	v_mfma_f32_32x32x64_f8f6f4 v[20:35], v[164:171], v[148:155], v[20:35]
	v_mfma_f32_32x32x64_f8f6f4 v[4:19], v[80:87], v[72:79], v[4:19]
	v_mfma_f32_32x32x64_f8f6f4 v[20:35], v[58:65], v[72:79], v[20:35]
	s_waitcnt lgkmcnt(0)
	v_or_b32_e32 v0, v39, v38
	v_or_b32_e32 v0, v40, v0
	v_or_b32_e32 v0, v41, v0
	v_or_b32_e32 v0, v42, v0
	v_or_b32_e32 v0, v43, v0
	v_or_b32_e32 v0, v44, v0
	v_or_b32_e32 v0, v45, v0
	v_cmp_ne_u32_e32 vcc, 0, v0
	s_cbranch_vccnz .LBB1_13
	s_mov_b64 s[0:1], -1
	s_nop 7
	v_mov_b64_e32 v[54:55], v[4:5]
	v_mov_b64_e32 v[56:57], v[6:7]
	v_mov_b64_e32 v[58:59], v[8:9]
	v_mov_b64_e32 v[60:61], v[10:11]
	v_mov_b64_e32 v[62:63], v[12:13]
	v_mov_b64_e32 v[64:65], v[14:15]
	v_mov_b64_e32 v[66:67], v[16:17]
	v_mov_b64_e32 v[68:69], v[18:19]
	v_mov_b64_e32 v[38:39], v[20:21]
	v_mov_b64_e32 v[40:41], v[22:23]
	v_mov_b64_e32 v[42:43], v[24:25]
	v_mov_b64_e32 v[44:45], v[26:27]
	v_mov_b64_e32 v[46:47], v[28:29]
	v_mov_b64_e32 v[48:49], v[30:31]
	v_mov_b64_e32 v[50:51], v[32:33]
	v_mov_b64_e32 v[52:53], v[34:35]
	s_branch .Lfinal_copy
